# MoE unit scheduler next(): 16 dependent LDS round trips per unit replaced by one lane-parallel read + compare + popcount (ph4, ph5 in-loop)
# speedup vs baseline: 1.0184x; 1.0184x over previous
;     __device__ __forceinline__ bool next(int i, Unit& u) const {
;         const int L = i * G + vcu; if (L >= total) return false;
;         const int mt = L / NN; u.pn = L - mt * NN; u.pm = mt;
;         int e = 0;
;         for (int j = 1; j < NEXP; ++j) e += (tb[j] <= mt) ? 1 : 0;
;         u.e = e; u.aux = mt - tb[e]; return true;
.LBB0_559:
	s_add_i32 s74, s18, 1
	v_readlane_b32 s2, v252, 7
	s_mul_i32 s2, s74, s2
	s_add_i32 s2, s2, s97
	s_cmp_lt_i32 s2, s26
	s_cselect_b64 s[22:23], -1, 0
	s_cmp_ge_i32 s2, s26
	s_cbranch_scc1 .LBB0_561
	s_ashr_i32 s3, s2, 31
	s_lshr_b32 s3, s3, 29
	s_add_i32 s3, s2, s3
	s_ashr_i32 s73, s3, 3
	s_and_b32 s3, s3, -8
	s_sub_i32 s20, s2, s3
	v_mbcnt_lo_u32_b32 v1, -1, 0
	v_mbcnt_hi_u32_b32 v1, -1, v1
	v_and_b32_e32 v1, 31, v1
	v_lshlrev_b32_e32 v1, 2, v1
	v_add_u32_e32 v1, 0x200c0, v1
	ds_read_b32 v6, v1
	s_waitcnt lgkmcnt(0)
	v_cmp_ge_i32_e32 vcc, s73, v6
	s_nop 1
	s_and_b32 s2, vcc_lo, -2
	s_bcnt1_i32_b32 s2, s2
	s_nop 3
	v_readlane_b32 s3, v6, s2
	v_mov_b32_e32 v208, s2
	s_nop 3
	s_sub_i32 s3, s73, s3
	s_nop 0
	v_mov_b32_e32 v243, s3

;     __device__ __forceinline__ bool next(int i, Unit& u) const {
;         const int L = i * G + vcu; if (L >= total) return false;
;         const int mt = L / NN; u.pn = L - mt * NN; u.pm = mt;
;         int e = 0;
;         for (int j = 1; j < NEXP; ++j) e += (tb[j] <= mt) ? 1 : 0;
;         u.e = e; u.aux = mt - tb[e]; return true;
.LBB0_639:
	s_add_i32 s57, s15, 1
	s_mul_i32 s2, s57, s72
	s_add_i32 s2, s2, s97
	s_cmp_lt_i32 s2, s26
	s_cselect_b64 s[24:25], -1, 0
	s_cmp_ge_i32 s2, s26
	s_cbranch_scc1 .LBB0_641
	s_ashr_i32 s3, s2, 31
	s_lshr_b32 s3, s3, 30
	s_add_i32 s3, s2, s3
	s_ashr_i32 s14, s3, 2
	s_and_b32 s3, s3, -4
	s_sub_i32 s16, s2, s3
	v_mbcnt_lo_u32_b32 v3, -1, 0
	v_mbcnt_hi_u32_b32 v3, -1, v3
	v_and_b32_e32 v3, 31, v3
	v_lshlrev_b32_e32 v3, 2, v3
	v_add_u32_e32 v3, 0x200c0, v3
	ds_read_b32 v4, v3
	s_waitcnt lgkmcnt(0)
	v_cmp_ge_i32_e32 vcc, s14, v4
	s_nop 1
	s_and_b32 s2, vcc_lo, -2
	s_bcnt1_i32_b32 s2, s2
	s_nop 0
	v_mov_b32_e32 v176, s2
